# speedup vs baseline: 1.0054x; 1.0054x over previous
.Lqkv_check:
	v_cmp_ne_u32_e32 vcc, 1, v240
	s_cmp_eq_u64 vcc, 0
	s_cbranch_scc1 .Lqkv_nopoll
	s_sleep 16
	s_add_i32 s83, s83, 1
	s_cmpk_lt_u32 s83, 0x1000
	s_cbranch_scc1 .Lqkv_poll
